# in-proj tail-fill Q=10, attention quotas 17/17 + balance deltas
# speedup vs baseline: 1.0128x; 1.0004x over previous
; #define LAS __attribute__((address_space(3)))
; #define PHASE_BEGIN() Ctx c = c0; { int t_ = c0.tid; asm volatile("" : "+v"(t_)); c.tid = t_; c.lane = t_ & 63; c.wave = __builtin_amdgcn_readfirstlane(t_ >> 6); } \
;     GAS unsigned char* wsb = (GAS unsigned char*)a.ws; asm volatile("" : "+s"(wsb));
; #define SEAM(k) do { if (IN(k) && IN((k) + 1)) { XcdBarrier b_ = bar; { GAS unsigned* t_ = (GAS unsigned*)b_.bar; asm volatile("" : "+s"(t_)); b_.bar = (unsigned*)t_; } xcd_barrier(b_); } } while (0)
; __device__ __forceinline__ void bg_take(const Args& a, const Ctx& c0, int n) {
;     PHASE_BEGIN();
;     unsigned* head = WSP(unsigned, WS_CTL) + CW_QHEAD;
;     volatile LAS unsigned* bc = (volatile LAS unsigned*)(c.lds + LDS_MISC + 64);
;     LAS float* scr = (LAS float*)(c.lds + c.wave * 16640);
;     __syncthreads();
;     for (int i = 0; i < n; ++i) {
;         if (c.tid == 0) { unsigned s = __hip_atomic_fetch_add(head, 1u, __ATOMIC_RELAXED, __HIP_MEMORY_SCOPE_AGENT); if (s >= (unsigned)BG_STEPS) s = 0xffffffffu; bc[0] = s; }
; __global__ void __launch_bounds__(512, 2) mk_fwd(Args a) {
;     ...
;             pg8::gemm_phase(c.lds, p); }
;     ...
;         if (IN(pb + 1)) bg_fill(a, c, l * 8 + 1, 0);
;     ...
;         SEAM(pb + 1);
.LBB0_322:
	v_readlane_b32 s2, v255, 42
	s_nop 3
	s_cmp_lg_u32 s2, 0
	s_cbranch_scc1 .Ltail_ret
	s_cmp_lt_u32 s90, 48
	s_cbranch_scc1 .Ltail_cont
	v_writelane_b32 v255, 1, 42
	s_mov_b32 s30, 0xc3e00000
	s_movk_i32 s78, 0x315c
	v_readlane_b32 s76, v254, 53
	s_mov_b32 s81, 0x10000
	s_mov_b32 s82, 0x18000
	s_mov_b32 s83, 0x8000
	s_mov_b32 s86, 0xc000
	s_mov_b32 s14, 10
	s_branch .Lbt1_entry

; __global__ void __launch_bounds__(512, 2) mk_fwd(Args a) {
;     ...
;         if (IN(pb + 5) && (c.bid & 1) == 0) { if (l == 0) mod_items(a, c, 1); bg_take(a, c, l == 0 ? 26 : 24); }
;         if (EN(5) && IN(pb + 5)) for (int rep = 0; rep < NREP(5); ++rep) { phase_attn(a, c, l, last); }
;         if (IN(pb + 5) && (c.bid & 1) == 1) { bg_take(a, c, l == 0 ? 26 : 24); if (l == 0) mod_items(a, c, 1); }
.LBB0_1254:
	s_cmp_lt_u32 s14, 25
	s_cbranch_scc1 .Lbal1_l1
	s_mov_b32 s14, 17
	s_cmp_lt_u32 s90, 32
	s_cbranch_scc0 .Lbal1_b
	s_add_i32 s14, s14, -4

; __global__ void __launch_bounds__(512, 2) mk_fwd(Args a) {
;     ...
;         if (IN(pb + 5) && (c.bid & 1) == 0) { if (l == 0) mod_items(a, c, 1); bg_take(a, c, l == 0 ? 26 : 24); }
;         if (EN(5) && IN(pb + 5)) for (int rep = 0; rep < NREP(5); ++rep) { phase_attn(a, c, l, last); }
;         if (IN(pb + 5) && (c.bid & 1) == 1) { bg_take(a, c, l == 0 ? 26 : 24); if (l == 0) mod_items(a, c, 1); }
.Lbal1_l1:
	s_mov_b32 s14, 17

; __global__ void __launch_bounds__(512, 2) mk_fwd(Args a) {
;     ...
;         if (IN(pb + 5) && (c.bid & 1) == 0) { if (l == 0) mod_items(a, c, 1); bg_take(a, c, l == 0 ? 26 : 24); }
;         if (EN(5) && IN(pb + 5)) for (int rep = 0; rep < NREP(5); ++rep) { phase_attn(a, c, l, last); }
;         if (IN(pb + 5) && (c.bid & 1) == 1) { bg_take(a, c, l == 0 ? 26 : 24); if (l == 0) mod_items(a, c, 1); }
.LBB0_1493:
	v_readlane_b32 s2, v252, 54
	v_readlane_b32 s3, v252, 55
	s_andn2_b64 vcc, exec, s[2:3]
	s_cbranch_vccnz .LBB0_1700
	v_readlane_b32 s2, v254, 54
	v_readlane_b32 s3, v254, 55
	s_and_b64 s[2:3], s[2:3], exec
	v_mov_b32_e32 v1, v0
	v_readlane_b32 s4, v254, 21
	v_readlane_b32 s5, v254, 22
	v_readfirstlane_b32 s2, v1
	v_readlane_b32 s6, v254, 23
	v_readlane_b32 s7, v254, 24
	s_cselect_b32 s10, 26, 24
	s_cmp_lt_u32 s10, 25
	s_cbranch_scc1 .Lbal2_l1
	s_mov_b32 s10, 17
	s_cmp_lt_u32 s90, 32
	s_cbranch_scc0 .Lbal2_b
	s_add_i32 s10, s10, -4

; __global__ void __launch_bounds__(512, 2) mk_fwd(Args a) {
;     ...
;         if (IN(pb + 5) && (c.bid & 1) == 0) { if (l == 0) mod_items(a, c, 1); bg_take(a, c, l == 0 ? 26 : 24); }
;         if (EN(5) && IN(pb + 5)) for (int rep = 0; rep < NREP(5); ++rep) { phase_attn(a, c, l, last); }
;         if (IN(pb + 5) && (c.bid & 1) == 1) { bg_take(a, c, l == 0 ? 26 : 24); if (l == 0) mod_items(a, c, 1); }
.Lbal2_l1:
	s_mov_b32 s10, 17
